# speedup vs baseline: 1.0393x; 1.0188x over previous
_Z11prep_kernelPKfS0_S0_S0_S0_S0_S0_S0_S0_PKiPDv8_DF16bS4_PfS5_S5_PiPt:
	s_load_dwordx4 s[16:19], s[0:1], 0x0
	s_load_dwordx4 s[20:23], s[0:1], 0x10
	s_load_dwordx4 s[24:27], s[0:1], 0x20
	s_load_dwordx4 s[28:31], s[0:1], 0x30
	s_load_dwordx4 s[32:35], s[0:1], 0x40
	s_load_dwordx2 s[36:37], s[0:1], 0x80
	v_and_b32_e32 v126, 63, v0
	v_lshrrev_b32_e32 v128, 6, v0
	v_and_b32_e32 v1, 15, v0
	v_bfe_u32 v24, v0, 4, 2
	v_lshl_or_b32 v107, v128, 4, v1
	v_lshlrev_b32_e32 v106, 2, v107
	v_lshlrev_b32_e32 v127, 2, v0
	v_lshlrev_b32_e32 v25, 1, v107
	v_and_b32_e32 v26, 48, v0
	v_mul_u32_u24_e32 v27, 0x440, v24
	v_lshlrev_b32_e32 v232, 4, v0
	v_lshrrev_b32_e32 v58, 5, v0
	v_mul_u32_u24_e32 v58, 0x110, v58
	v_and_b32_e32 v239, 31, v0
	v_lshl_add_u32 v58, v239, 3, v58
	v_add_u32_e32 v238, 0x1b400, v58
	v_mul_u32_u24_e32 v52, 0x110, v1
	v_add_u32_e32 v52, v52, v26
	v_add_u32_e32 v53, 0x1b400, v52
	v_add_u32_e32 v54, 0x1c500, v52
	v_add_u32_e32 v55, v27, v25
	v_add_u32_e32 v55, 0x1c500, v55
	v_mul_u32_u24_e32 v56, 0x110, v107
	v_add_u32_e32 v56, v56, v26
	v_add_u32_e32 v57, 0x8800, v56
	s_lshl_b32 s12, s2, 4
	s_add_i32 s3, s12, 0xfffff800
	s_cmpk_gt_i32 s2, 0x7f
	s_cselect_b64 s[6:7], -1, 0
	s_mov_b32 s48, 0
	s_mov_b32 s49, -1
	v_lshl_or_b32 v236, s2, 3, v128
	v_lshlrev_b32_e32 v236, 12, v236
	v_lshl_add_u32 v236, v126, 4, v236
	s_waitcnt lgkmcnt(0)
	s_cmpk_lt_i32 s2, 0x80
	s_cselect_b32 s38, s16, s18
	s_cselect_b32 s39, s17, s19
	s_cselect_b32 s40, s20, s24
	s_cselect_b32 s41, s21, s25
	s_cselect_b32 s13, s12, s3
	s_cselect_b32 s44, 0x3db504f3, 1.0
	s_lshl_b32 s13, s13, 9
	s_add_u32 s38, s38, s13
	s_addc_u32 s39, s39, 0
	global_load_dwordx4 v[2:5], v232, s[38:39] nt
	s_and_b32 s13, s2, 7
	s_lshl_b32 s14, s13, 13
	v_add_u32_e32 v239, s14, v232
	global_load_dwordx4 v[132:135], v239, s[40:41]
	s_add_i32 s13, s2, 1
	s_and_b32 s13, s13, 7
	s_lshl_b32 s14, s13, 13
	v_add_u32_e32 v239, s14, v232
	global_load_dwordx4 v[136:139], v239, s[40:41]
	s_add_i32 s13, s2, 2
	s_and_b32 s13, s13, 7
	s_lshl_b32 s14, s13, 13
	v_add_u32_e32 v239, s14, v232
	global_load_dwordx4 v[140:143], v239, s[40:41]
	s_add_i32 s13, s2, 3
	s_and_b32 s13, s13, 7
	s_lshl_b32 s14, s13, 13
	v_add_u32_e32 v239, s14, v232
	global_load_dwordx4 v[144:147], v239, s[40:41]
	s_add_i32 s13, s2, 4
	s_and_b32 s13, s13, 7
	s_lshl_b32 s14, s13, 13
	v_add_u32_e32 v239, s14, v232
	global_load_dwordx4 v[148:151], v239, s[40:41]
	s_add_i32 s13, s2, 5
	s_and_b32 s13, s13, 7
	s_lshl_b32 s14, s13, 13
	v_add_u32_e32 v239, s14, v232
	global_load_dwordx4 v[152:155], v239, s[40:41]
	s_add_i32 s13, s2, 6
	s_and_b32 s13, s13, 7
	s_lshl_b32 s14, s13, 13
	v_add_u32_e32 v239, s14, v232
	global_load_dwordx4 v[156:159], v239, s[40:41]
	s_add_i32 s13, s2, 7
	s_and_b32 s13, s13, 7
	s_lshl_b32 s14, s13, 13
	v_add_u32_e32 v239, s14, v232
	global_load_dwordx4 v[160:163], v239, s[40:41]
	global_load_dword v129, v106, s[32:33]
	global_load_dword v130, v106, s[30:31]
	s_and_b64 vcc, exec, s[6:7]
	s_cbranch_vccz .Lp_q
	v_cmp_gt_u32_e32 vcc, 32, v126
	v_mov_b32_e32 v244, 0x3db504f3
	v_mov_b32_e32 v239, s22
	v_mov_b32_e32 v240, s26
	v_cndmask_b32_e32 v244, 1.0, v244, vcc
	v_cndmask_b32_e32 v240, v240, v239, vcc
	v_mov_b32_e32 v239, s23
	v_mov_b32_e32 v241, s27
	v_cndmask_b32_e32 v241, v241, v239, vcc
	v_and_b32_e32 v242, 31, v126
	v_lshlrev_b32_e32 v242, 4, v242
	v_mov_b32_e32 v243, 0
	v_lshl_add_u64 v[240:241], v[240:241], 0, v[242:243]
	global_load_dwordx4 v[228:231], v[240:241], off
	v_lshlrev_b32_e32 v233, 14, v128
	v_lshl_add_u32 v233, v126, 4, v233
	s_and_b32 s13, s2, 15
	s_lshl_b32 s14, s13, 10
	s_add_u32 s46, s28, s14
	s_addc_u32 s47, s29, 0
	global_load_dwordx4 v[164:167], v233, s[46:47]
	s_add_i32 s13, s2, 1
	s_and_b32 s13, s13, 15
	s_lshl_b32 s14, s13, 10
	s_add_u32 s46, s28, s14
	s_addc_u32 s47, s29, 0
	global_load_dwordx4 v[168:171], v233, s[46:47]
	s_add_i32 s13, s2, 2
	s_and_b32 s13, s13, 15
	s_lshl_b32 s14, s13, 10
	s_add_u32 s46, s28, s14
	s_addc_u32 s47, s29, 0
	global_load_dwordx4 v[172:175], v233, s[46:47]
	s_add_i32 s13, s2, 3
	s_and_b32 s13, s13, 15
	s_lshl_b32 s14, s13, 10
	s_add_u32 s46, s28, s14
	s_addc_u32 s47, s29, 0
	global_load_dwordx4 v[176:179], v233, s[46:47]
	s_add_i32 s13, s2, 4
	s_and_b32 s13, s13, 15
	s_lshl_b32 s14, s13, 10
	s_add_u32 s46, s28, s14
	s_addc_u32 s47, s29, 0
	global_load_dwordx4 v[180:183], v233, s[46:47]
	s_add_i32 s13, s2, 5
	s_and_b32 s13, s13, 15
	s_lshl_b32 s14, s13, 10
	s_add_u32 s46, s28, s14
	s_addc_u32 s47, s29, 0
	global_load_dwordx4 v[184:187], v233, s[46:47]
	s_add_i32 s13, s2, 6
	s_and_b32 s13, s13, 15
	s_lshl_b32 s14, s13, 10
	s_add_u32 s46, s28, s14
	s_addc_u32 s47, s29, 0
	global_load_dwordx4 v[188:191], v233, s[46:47]
	s_add_i32 s13, s2, 7
	s_and_b32 s13, s13, 15
	s_lshl_b32 s14, s13, 10
	s_add_u32 s46, s28, s14
	s_addc_u32 s47, s29, 0
	global_load_dwordx4 v[192:195], v233, s[46:47]
	s_add_i32 s13, s2, 8
	s_and_b32 s13, s13, 15
	s_lshl_b32 s14, s13, 10
	s_add_u32 s46, s28, s14
	s_addc_u32 s47, s29, 0
	global_load_dwordx4 v[196:199], v233, s[46:47]
	s_add_i32 s13, s2, 9
	s_and_b32 s13, s13, 15
	s_lshl_b32 s14, s13, 10
	s_add_u32 s46, s28, s14
	s_addc_u32 s47, s29, 0
	global_load_dwordx4 v[200:203], v233, s[46:47]
	s_add_i32 s13, s2, 10
	s_and_b32 s13, s13, 15
	s_lshl_b32 s14, s13, 10
	s_add_u32 s46, s28, s14
	s_addc_u32 s47, s29, 0
	global_load_dwordx4 v[204:207], v233, s[46:47]
	s_add_i32 s13, s2, 11
	s_and_b32 s13, s13, 15
	s_lshl_b32 s14, s13, 10
	s_add_u32 s46, s28, s14
	s_addc_u32 s47, s29, 0
	global_load_dwordx4 v[208:211], v233, s[46:47]
	s_add_i32 s13, s2, 12
	s_and_b32 s13, s13, 15
	s_lshl_b32 s14, s13, 10
	s_add_u32 s46, s28, s14
	s_addc_u32 s47, s29, 0
	global_load_dwordx4 v[212:215], v233, s[46:47]
	s_add_i32 s13, s2, 13
	s_and_b32 s13, s13, 15
	s_lshl_b32 s14, s13, 10
	s_add_u32 s46, s28, s14
	s_addc_u32 s47, s29, 0
	global_load_dwordx4 v[216:219], v233, s[46:47]
	s_add_i32 s13, s2, 14
	s_and_b32 s13, s13, 15
	s_lshl_b32 s14, s13, 10
	s_add_u32 s46, s28, s14
	s_addc_u32 s47, s29, 0
	global_load_dwordx4 v[220:223], v233, s[46:47]
	s_add_i32 s13, s2, 15
	s_and_b32 s13, s13, 15
	s_lshl_b32 s14, s13, 10
	s_add_u32 s46, s28, s14
	s_addc_u32 s47, s29, 0
	global_load_dwordx4 v[224:227], v233, s[46:47]
	v_mul_u32_u24_e32 v59, 0x1040, v128
	v_lshl_add_u32 v59, v126, 2, v59
	v_add_u32_e32 v59, 0x11000, v59
	v_mul_u32_u24_e32 v76, 0x1100, v128
	v_lshl_add_u32 v76, v126, 3, v76
	v_add_u32_e32 v76, 0x8700, v76
	v_lshrrev_b32_e32 v77, 2, v126
	v_mul_u32_u24_e32 v77, 0x104, v77
	v_mul_u32_u24_e32 v239, 0x1040, v128
	v_add_u32_e32 v77, v77, v239
	v_and_b32_e32 v239, 3, v126
	v_lshl_add_u32 v77, v239, 6, v77
	v_add_u32_e32 v77, 0x11000, v77
	s_waitcnt vmcnt(27)
	v_cvt_pk_bf16_f32 v12, v2, v3
	v_cvt_pk_bf16_f32 v13, v4, v5
	ds_write_b64 v238, v[12:13]
	s_waitcnt vmcnt(26)
	v_cvt_pk_bf16_f32 v6, v132, v133
	v_cvt_pk_bf16_f32 v7, v134, v135
	s_and_b32 s13, s2, 7
	s_mul_i32 s14, s13, 0x1100
	v_add_u32_e32 v239, s14, v58
	ds_write_b64 v239, v[6:7]
	s_waitcnt vmcnt(25)
	v_cvt_pk_bf16_f32 v8, v136, v137
	v_cvt_pk_bf16_f32 v9, v138, v139
	s_add_i32 s13, s2, 1
	s_and_b32 s13, s13, 7
	s_mul_i32 s14, s13, 0x1100
	v_add_u32_e32 v10, s14, v58
	ds_write_b64 v10, v[8:9]
	s_waitcnt vmcnt(24)
	v_cvt_pk_bf16_f32 v6, v140, v141
	v_cvt_pk_bf16_f32 v7, v142, v143
	s_add_i32 s13, s2, 2
	s_and_b32 s13, s13, 7
	s_mul_i32 s14, s13, 0x1100
	v_add_u32_e32 v239, s14, v58
	ds_write_b64 v239, v[6:7]
	s_waitcnt vmcnt(23)
	v_cvt_pk_bf16_f32 v8, v144, v145
	v_cvt_pk_bf16_f32 v9, v146, v147
	s_add_i32 s13, s2, 3
	s_and_b32 s13, s13, 7
	s_mul_i32 s14, s13, 0x1100
	v_add_u32_e32 v10, s14, v58
	ds_write_b64 v10, v[8:9]
	s_waitcnt vmcnt(22)
	v_cvt_pk_bf16_f32 v6, v148, v149
	v_cvt_pk_bf16_f32 v7, v150, v151
	s_add_i32 s13, s2, 4
	s_and_b32 s13, s13, 7
	s_mul_i32 s14, s13, 0x1100
	v_add_u32_e32 v239, s14, v58
	ds_write_b64 v239, v[6:7]
	s_waitcnt vmcnt(21)
	v_cvt_pk_bf16_f32 v8, v152, v153
	v_cvt_pk_bf16_f32 v9, v154, v155
	s_add_i32 s13, s2, 5
	s_and_b32 s13, s13, 7
	s_mul_i32 s14, s13, 0x1100
	v_add_u32_e32 v10, s14, v58
	ds_write_b64 v10, v[8:9]
	s_waitcnt vmcnt(20)
	v_cvt_pk_bf16_f32 v6, v156, v157
	v_cvt_pk_bf16_f32 v7, v158, v159
	s_add_i32 s13, s2, 6
	s_and_b32 s13, s13, 7
	s_mul_i32 s14, s13, 0x1100
	v_add_u32_e32 v239, s14, v58
	ds_write_b64 v239, v[6:7]
	s_waitcnt vmcnt(19)
	v_cvt_pk_bf16_f32 v8, v160, v161
	v_cvt_pk_bf16_f32 v9, v162, v163
	s_add_i32 s13, s2, 7
	s_and_b32 s13, s13, 7
	s_mul_i32 s14, s13, 0x1100
	v_add_u32_e32 v10, s14, v58
	ds_write_b64 v10, v[8:9]
	s_waitcnt vmcnt(16)
	v_pk_mul_f32 v[228:229], v[244:245], v[228:229] op_sel_hi:[0,1]
	v_pk_mul_f32 v[230:231], v[244:245], v[230:231] op_sel_hi:[0,1]
	s_waitcnt vmcnt(15)
	v_mul_f32_e32 v6, v229, v165
	v_mul_f32_e32 v7, v231, v167
	v_fmac_f32_e32 v6, v228, v164
	v_fmac_f32_e32 v7, v230, v166
	s_and_b32 s13, s2, 15
	s_mul_i32 s14, s13, 0x104
	s_mul_i32 s15, s13, 0x110
	v_add_f32_e32 v6, v6, v7
	v_add_u32_e32 v239, s14, v59
	ds_write_b32 v239, v6
	v_cvt_pk_bf16_f32 v8, v164, v165
	v_cvt_pk_bf16_f32 v9, v166, v167
	v_add_u32_e32 v10, s15, v76
	s_mov_b64 exec, s[48:49]
	ds_write_b64 v10, v[8:9]
	s_mov_b64 exec, -1
	s_waitcnt vmcnt(14)
	v_mul_f32_e32 v11, v229, v169
	v_mul_f32_e32 v15, v231, v171
	v_fmac_f32_e32 v11, v228, v168
	v_fmac_f32_e32 v15, v230, v170
	s_add_i32 s13, s2, 1
	s_and_b32 s13, s13, 15
	s_mul_i32 s14, s13, 0x104
	s_mul_i32 s15, s13, 0x110
	v_add_f32_e32 v11, v11, v15
	v_add_u32_e32 v16, s14, v59
	ds_write_b32 v16, v11
	v_cvt_pk_bf16_f32 v12, v168, v169
	v_cvt_pk_bf16_f32 v13, v170, v171
	v_add_u32_e32 v14, s15, v76
	s_mov_b64 exec, s[48:49]
	ds_write_b64 v14, v[12:13]
	s_mov_b64 exec, -1
	s_waitcnt vmcnt(13)
	v_mul_f32_e32 v6, v229, v173
	v_mul_f32_e32 v7, v231, v175
	v_fmac_f32_e32 v6, v228, v172
	v_fmac_f32_e32 v7, v230, v174
	s_add_i32 s13, s2, 2
	s_and_b32 s13, s13, 15
	s_mul_i32 s14, s13, 0x104
	s_mul_i32 s15, s13, 0x110
	v_add_f32_e32 v6, v6, v7
	v_add_u32_e32 v239, s14, v59
	ds_write_b32 v239, v6
	v_cvt_pk_bf16_f32 v8, v172, v173
	v_cvt_pk_bf16_f32 v9, v174, v175
	v_add_u32_e32 v10, s15, v76
	s_mov_b64 exec, s[48:49]
	ds_write_b64 v10, v[8:9]
	s_mov_b64 exec, -1
	s_waitcnt vmcnt(12)
	v_mul_f32_e32 v11, v229, v177
	v_mul_f32_e32 v15, v231, v179
	v_fmac_f32_e32 v11, v228, v176
	v_fmac_f32_e32 v15, v230, v178
	s_add_i32 s13, s2, 3
	s_and_b32 s13, s13, 15
	s_mul_i32 s14, s13, 0x104
	s_mul_i32 s15, s13, 0x110
	v_add_f32_e32 v11, v11, v15
	v_add_u32_e32 v16, s14, v59
	ds_write_b32 v16, v11
	v_cvt_pk_bf16_f32 v12, v176, v177
	v_cvt_pk_bf16_f32 v13, v178, v179
	v_add_u32_e32 v14, s15, v76
	s_mov_b64 exec, s[48:49]
	ds_write_b64 v14, v[12:13]
	s_mov_b64 exec, -1
	s_waitcnt vmcnt(11)
	v_mul_f32_e32 v6, v229, v181
	v_mul_f32_e32 v7, v231, v183
	v_fmac_f32_e32 v6, v228, v180
	v_fmac_f32_e32 v7, v230, v182
	s_add_i32 s13, s2, 4
	s_and_b32 s13, s13, 15
	s_mul_i32 s14, s13, 0x104
	s_mul_i32 s15, s13, 0x110
	v_add_f32_e32 v6, v6, v7
	v_add_u32_e32 v239, s14, v59
	ds_write_b32 v239, v6
	v_cvt_pk_bf16_f32 v8, v180, v181
	v_cvt_pk_bf16_f32 v9, v182, v183
	v_add_u32_e32 v10, s15, v76
	s_mov_b64 exec, s[48:49]
	ds_write_b64 v10, v[8:9]
	s_mov_b64 exec, -1
	s_waitcnt vmcnt(10)
	v_mul_f32_e32 v11, v229, v185
	v_mul_f32_e32 v15, v231, v187
	v_fmac_f32_e32 v11, v228, v184
	v_fmac_f32_e32 v15, v230, v186
	s_add_i32 s13, s2, 5
	s_and_b32 s13, s13, 15
	s_mul_i32 s14, s13, 0x104
	s_mul_i32 s15, s13, 0x110
	v_add_f32_e32 v11, v11, v15
	v_add_u32_e32 v16, s14, v59
	ds_write_b32 v16, v11
	v_cvt_pk_bf16_f32 v12, v184, v185
	v_cvt_pk_bf16_f32 v13, v186, v187
	v_add_u32_e32 v14, s15, v76
	s_mov_b64 exec, s[48:49]
	ds_write_b64 v14, v[12:13]
	s_mov_b64 exec, -1
	s_waitcnt vmcnt(9)
	v_mul_f32_e32 v6, v229, v189
	v_mul_f32_e32 v7, v231, v191
	v_fmac_f32_e32 v6, v228, v188
	v_fmac_f32_e32 v7, v230, v190
	s_add_i32 s13, s2, 6
	s_and_b32 s13, s13, 15
	s_mul_i32 s14, s13, 0x104
	s_mul_i32 s15, s13, 0x110
	v_add_f32_e32 v6, v6, v7
	v_add_u32_e32 v239, s14, v59
	ds_write_b32 v239, v6
	v_cvt_pk_bf16_f32 v8, v188, v189
	v_cvt_pk_bf16_f32 v9, v190, v191
	v_add_u32_e32 v10, s15, v76
	s_mov_b64 exec, s[48:49]
	ds_write_b64 v10, v[8:9]
	s_mov_b64 exec, -1
	s_waitcnt vmcnt(8)
	v_mul_f32_e32 v11, v229, v193
	v_mul_f32_e32 v15, v231, v195
	v_fmac_f32_e32 v11, v228, v192
	v_fmac_f32_e32 v15, v230, v194
	s_add_i32 s13, s2, 7
	s_and_b32 s13, s13, 15
	s_mul_i32 s14, s13, 0x104
	s_mul_i32 s15, s13, 0x110
	v_add_f32_e32 v11, v11, v15
	v_add_u32_e32 v16, s14, v59
	ds_write_b32 v16, v11
	v_cvt_pk_bf16_f32 v12, v192, v193
	v_cvt_pk_bf16_f32 v13, v194, v195
	v_add_u32_e32 v14, s15, v76
	s_mov_b64 exec, s[48:49]
	ds_write_b64 v14, v[12:13]
	s_mov_b64 exec, -1
	s_waitcnt vmcnt(7)
	v_mul_f32_e32 v6, v229, v197
	v_mul_f32_e32 v7, v231, v199
	v_fmac_f32_e32 v6, v228, v196
	v_fmac_f32_e32 v7, v230, v198
	s_add_i32 s13, s2, 8
	s_and_b32 s13, s13, 15
	s_mul_i32 s14, s13, 0x104
	s_mul_i32 s15, s13, 0x110
	v_add_f32_e32 v6, v6, v7
	v_add_u32_e32 v239, s14, v59
	ds_write_b32 v239, v6
	v_cvt_pk_bf16_f32 v8, v196, v197
	v_cvt_pk_bf16_f32 v9, v198, v199
	v_add_u32_e32 v10, s15, v76
	s_mov_b64 exec, s[48:49]
	ds_write_b64 v10, v[8:9]
	s_mov_b64 exec, -1
	s_waitcnt vmcnt(6)
	v_mul_f32_e32 v11, v229, v201
	v_mul_f32_e32 v15, v231, v203
	v_fmac_f32_e32 v11, v228, v200
	v_fmac_f32_e32 v15, v230, v202
	s_add_i32 s13, s2, 9
	s_and_b32 s13, s13, 15
	s_mul_i32 s14, s13, 0x104
	s_mul_i32 s15, s13, 0x110
	v_add_f32_e32 v11, v11, v15
	v_add_u32_e32 v16, s14, v59
	ds_write_b32 v16, v11
	v_cvt_pk_bf16_f32 v12, v200, v201
	v_cvt_pk_bf16_f32 v13, v202, v203
	v_add_u32_e32 v14, s15, v76
	s_mov_b64 exec, s[48:49]
	ds_write_b64 v14, v[12:13]
	s_mov_b64 exec, -1
	s_waitcnt vmcnt(5)
	v_mul_f32_e32 v6, v229, v205
	v_mul_f32_e32 v7, v231, v207
	v_fmac_f32_e32 v6, v228, v204
	v_fmac_f32_e32 v7, v230, v206
	s_add_i32 s13, s2, 10
	s_and_b32 s13, s13, 15
	s_mul_i32 s14, s13, 0x104
	s_mul_i32 s15, s13, 0x110
	v_add_f32_e32 v6, v6, v7
	v_add_u32_e32 v239, s14, v59
	ds_write_b32 v239, v6
	v_cvt_pk_bf16_f32 v8, v204, v205
	v_cvt_pk_bf16_f32 v9, v206, v207
	v_add_u32_e32 v10, s15, v76
	s_mov_b64 exec, s[48:49]
	ds_write_b64 v10, v[8:9]
	s_mov_b64 exec, -1
	s_waitcnt vmcnt(4)
	v_mul_f32_e32 v11, v229, v209
	v_mul_f32_e32 v15, v231, v211
	v_fmac_f32_e32 v11, v228, v208
	v_fmac_f32_e32 v15, v230, v210
	s_add_i32 s13, s2, 11
	s_and_b32 s13, s13, 15
	s_mul_i32 s14, s13, 0x104
	s_mul_i32 s15, s13, 0x110
	v_add_f32_e32 v11, v11, v15
	v_add_u32_e32 v16, s14, v59
	ds_write_b32 v16, v11
	v_cvt_pk_bf16_f32 v12, v208, v209
	v_cvt_pk_bf16_f32 v13, v210, v211
	v_add_u32_e32 v14, s15, v76
	s_mov_b64 exec, s[48:49]
	ds_write_b64 v14, v[12:13]
	s_mov_b64 exec, -1
	s_waitcnt vmcnt(3)
	v_mul_f32_e32 v6, v229, v213
	v_mul_f32_e32 v7, v231, v215
	v_fmac_f32_e32 v6, v228, v212
	v_fmac_f32_e32 v7, v230, v214
	s_add_i32 s13, s2, 12
	s_and_b32 s13, s13, 15
	s_mul_i32 s14, s13, 0x104
	s_mul_i32 s15, s13, 0x110
	v_add_f32_e32 v6, v6, v7
	v_add_u32_e32 v239, s14, v59
	ds_write_b32 v239, v6
	v_cvt_pk_bf16_f32 v8, v212, v213
	v_cvt_pk_bf16_f32 v9, v214, v215
	v_add_u32_e32 v10, s15, v76
	s_mov_b64 exec, s[48:49]
	ds_write_b64 v10, v[8:9]
	s_mov_b64 exec, -1
	s_waitcnt vmcnt(2)
	v_mul_f32_e32 v11, v229, v217
	v_mul_f32_e32 v15, v231, v219
	v_fmac_f32_e32 v11, v228, v216
	v_fmac_f32_e32 v15, v230, v218
	s_add_i32 s13, s2, 13
	s_and_b32 s13, s13, 15
	s_mul_i32 s14, s13, 0x104
	s_mul_i32 s15, s13, 0x110
	v_add_f32_e32 v11, v11, v15
	v_add_u32_e32 v16, s14, v59
	ds_write_b32 v16, v11
	v_cvt_pk_bf16_f32 v12, v216, v217
	v_cvt_pk_bf16_f32 v13, v218, v219
	v_add_u32_e32 v14, s15, v76
	s_mov_b64 exec, s[48:49]
	ds_write_b64 v14, v[12:13]
	s_mov_b64 exec, -1
	s_waitcnt vmcnt(1)
	v_mul_f32_e32 v6, v229, v221
	v_mul_f32_e32 v7, v231, v223
	v_fmac_f32_e32 v6, v228, v220
	v_fmac_f32_e32 v7, v230, v222
	s_add_i32 s13, s2, 14
	s_and_b32 s13, s13, 15
	s_mul_i32 s14, s13, 0x104
	s_mul_i32 s15, s13, 0x110
	v_add_f32_e32 v6, v6, v7
	v_add_u32_e32 v239, s14, v59
	ds_write_b32 v239, v6
	v_cvt_pk_bf16_f32 v8, v220, v221
	v_cvt_pk_bf16_f32 v9, v222, v223
	v_add_u32_e32 v10, s15, v76
	s_mov_b64 exec, s[48:49]
	ds_write_b64 v10, v[8:9]
	s_mov_b64 exec, -1
	s_waitcnt vmcnt(0)
	v_mul_f32_e32 v11, v229, v225
	v_mul_f32_e32 v15, v231, v227
	v_fmac_f32_e32 v11, v228, v224
	v_fmac_f32_e32 v15, v230, v226
	s_add_i32 s13, s2, 15
	s_and_b32 s13, s13, 15
	s_mul_i32 s14, s13, 0x104
	s_mul_i32 s15, s13, 0x110
	v_add_f32_e32 v11, v11, v15
	v_add_u32_e32 v16, s14, v59
	ds_write_b32 v16, v11
	v_cvt_pk_bf16_f32 v12, v224, v225
	v_cvt_pk_bf16_f32 v13, v226, v227
	v_add_u32_e32 v14, s15, v76
	s_mov_b64 exec, s[48:49]
	ds_write_b64 v14, v[12:13]
	s_mov_b64 exec, -1
	s_waitcnt lgkmcnt(0)
	ds_read2_b32 v[60:61], v77 offset0:0 offset1:1
	ds_read2_b32 v[62:63], v77 offset0:2 offset1:3
	ds_read2_b32 v[64:65], v77 offset0:4 offset1:5
	ds_read2_b32 v[66:67], v77 offset0:6 offset1:7
	ds_read2_b32 v[68:69], v77 offset0:8 offset1:9
	ds_read2_b32 v[70:71], v77 offset0:10 offset1:11
	ds_read2_b32 v[72:73], v77 offset0:12 offset1:13
	ds_read2_b32 v[74:75], v77 offset0:14 offset1:15
	s_waitcnt lgkmcnt(0)
	v_add_f32_e32 v78, 0, v60
	v_add_f32_e32 v78, v78, v61
	v_add_f32_e32 v78, v78, v62
	v_add_f32_e32 v78, v78, v63
	v_add_f32_e32 v78, v78, v64
	v_add_f32_e32 v78, v78, v65
	v_add_f32_e32 v78, v78, v66
	v_add_f32_e32 v78, v78, v67
	v_add_f32_e32 v78, v78, v68
	v_add_f32_e32 v78, v78, v69
	v_add_f32_e32 v78, v78, v70
	v_add_f32_e32 v78, v78, v71
	v_add_f32_e32 v78, v78, v72
	v_add_f32_e32 v78, v78, v73
	v_add_f32_e32 v78, v78, v74
	v_add_f32_e32 v78, v78, v75
	s_nop 1
	v_add_f32_dpp v78, v78, v78 quad_perm:[1,0,3,2] row_mask:0xf bank_mask:0xf bound_ctrl:1
	s_nop 1
	v_add_f32_dpp v78, v78, v78 quad_perm:[2,3,0,1] row_mask:0xf bank_mask:0xf bound_ctrl:1
	v_lshlrev_b32_e32 v79, 4, v1
	ds_bpermute_b32 v78, v79, v78
	s_waitcnt lgkmcnt(0)
	s_barrier
	global_load_dwordx4 v[2:5], v236, s[34:35] nt
	global_load_dwordx4 v[6:9], v236, s[34:35] offset:1024 nt
	global_load_dwordx4 v[10:13], v236, s[34:35] offset:2048 nt
	global_load_dwordx4 v[14:17], v236, s[34:35] offset:3072 nt
	ds_read_b128 v[28:31], v53
	ds_read_b128 v[60:63], v56
	ds_read_b128 v[32:35], v53 offset:64
	ds_read_b128 v[64:67], v56 offset:64
	ds_read_b128 v[36:39], v53 offset:128
	ds_read_b128 v[68:71], v56 offset:128
	ds_read_b128 v[40:43], v53 offset:192
	ds_read_b128 v[72:75], v56 offset:192
	s_waitcnt lgkmcnt(6)
	v_mfma_f32_16x16x32_bf16 v[18:21], v[28:31], v[60:63], 0
	s_waitcnt lgkmcnt(4)
	v_mfma_f32_16x16x32_bf16 v[18:21], v[32:35], v[64:67], v[18:21]
	s_waitcnt lgkmcnt(2)
	v_mfma_f32_16x16x32_bf16 v[18:21], v[36:39], v[68:71], v[18:21]
	s_waitcnt lgkmcnt(0)
	v_mfma_f32_16x16x32_bf16 v[18:21], v[40:43], v[72:75], v[18:21]
	s_nop 7
	v_mul_f32_e32 v18, s44, v18
	v_mul_f32_e32 v19, s44, v19
	v_mul_f32_e32 v20, s44, v20
	v_mul_f32_e32 v21, s44, v21
	v_cvt_pk_bf16_f32 v18, v18, v18
	v_cvt_pk_bf16_f32 v19, v19, v19
	v_cvt_pk_bf16_f32 v20, v20, v20
	v_cvt_pk_bf16_f32 v21, v21, v21
	ds_write_b16 v55, v18
	ds_write_b16 v55, v19 offset:272
	ds_write_b16 v55, v20 offset:544
	ds_write_b16 v55, v21 offset:816
	s_waitcnt lgkmcnt(0)
	s_barrier
	ds_read_b128 v[28:31], v54
	ds_read_b128 v[60:63], v57
	ds_read_b128 v[32:35], v54 offset:64
	ds_read_b128 v[64:67], v57 offset:64
	ds_read_b128 v[36:39], v54 offset:128
	ds_read_b128 v[68:71], v57 offset:128
	ds_read_b128 v[40:43], v54 offset:192
	ds_read_b128 v[72:75], v57 offset:192
	s_waitcnt lgkmcnt(6)
	v_mfma_f32_16x16x32_bf16 v[18:21], v[28:31], v[60:63], 0
	s_waitcnt lgkmcnt(4)
	v_mfma_f32_16x16x32_bf16 v[18:21], v[32:35], v[64:67], v[18:21]
	s_waitcnt lgkmcnt(2)
	v_mfma_f32_16x16x32_bf16 v[18:21], v[36:39], v[68:71], v[18:21]
	s_waitcnt lgkmcnt(0)
	v_mfma_f32_16x16x32_bf16 v[18:21], v[40:43], v[72:75], v[18:21]
	s_nop 2
	v_mov_b32_e32 v28, v78
	s_load_dwordx2 s[4:5], s[0:1], 0x70
	v_lshl_or_b32 v30, v24, 2, s3
	v_ashrrev_i32_e32 v31, 31, v30
	v_mov_b32_e32 v107, 0
	s_waitcnt lgkmcnt(0)
	v_add_f32_e32 v34, v130, v28
	v_add_f32_e32 v35, v34, v18
	v_add_f32_e32 v28, v35, v35
	v_mul_f32_e32 v28, 0x3fb8aa3b, v28
	v_exp_f32_e32 v32, v28
	v_lshlrev_b64 v[28:29], 9, v[30:31]
	s_mov_b32 s8, 0x19200
	v_add3_u32 v37, v27, v25, s8
	v_add_f32_e32 v31, 1.0, v32
	v_rcp_f32_e32 v31, v31
	v_lshl_add_u64 v[32:33], s[4:5], 0, v[106:107]
	v_lshl_add_u64 v[28:29], v[32:33], 0, v[28:29]
	global_store_dword v[28:29], v35, off sc1
	v_fma_f32 v35, v31, -2.0, 1.0
	v_fma_f32 v28, -v35, v35, 1.0
	v_mul_f32_e32 v28, v129, v28
	v_add_f32_e32 v31, v34, v19
	v_cvt_pk_bf16_f32 v29, v28, s0
	v_mul_f32_e64 v27, v35, -v28
	v_add_f32_e32 v28, v31, v31
	v_mul_f32_e32 v28, 0x3fb8aa3b, v28
	v_exp_f32_e32 v38, v28
	v_cvt_pk_bf16_f32 v27, v27, s0
	ds_write_b16 v37, v27 offset:4352
	v_or_b32_e32 v28, 1, v30
	v_add_f32_e32 v27, 1.0, v38
	v_rcp_f32_e32 v27, v27
	ds_write_b16 v37, v29
	v_ashrrev_i32_e32 v29, 31, v28
	v_lshlrev_b64 v[28:29], 9, v[28:29]
	v_lshl_add_u64 v[28:29], v[32:33], 0, v[28:29]
	v_fma_f32 v27, v27, -2.0, 1.0
	global_store_dword v[28:29], v31, off sc1
	v_fma_f32 v28, -v27, v27, 1.0
	v_mul_f32_e32 v28, v129, v28
	v_cvt_pk_bf16_f32 v29, v28, s0
	v_add_f32_e32 v31, v34, v20
	ds_write_b16 v37, v29 offset:272
	v_add_f32_e32 v29, v31, v31
	v_mul_f32_e32 v29, 0x3fb8aa3b, v29
	v_exp_f32_e32 v38, v29
	v_mul_f32_e64 v28, v27, -v28
	v_cvt_pk_bf16_f32 v28, v28, s0
	ds_write_b16 v37, v28 offset:4624
	v_add_f32_e32 v38, 1.0, v38
	v_or_b32_e32 v28, 2, v30
	v_rcp_f32_e32 v38, v38
	v_ashrrev_i32_e32 v29, 31, v28
	v_lshlrev_b64 v[28:29], 9, v[28:29]
	v_lshl_add_u64 v[28:29], v[32:33], 0, v[28:29]
	global_store_dword v[28:29], v31, off sc1
	v_fma_f32 v28, v38, -2.0, 1.0
	v_fma_f32 v29, -v28, v28, 1.0
	v_mul_f32_e32 v29, v129, v29
	v_cvt_pk_bf16_f32 v31, v29, s0
	v_add_f32_e32 v34, v34, v21
	ds_write_b16 v37, v31 offset:544
	v_add_f32_e32 v31, v34, v34
	v_mul_f32_e32 v31, 0x3fb8aa3b, v31
	v_exp_f32_e32 v38, v31
	v_mul_f32_e64 v29, v28, -v29
	v_cvt_pk_bf16_f32 v29, v29, s0
	ds_write_b16 v37, v29 offset:4896
	v_add_f32_e32 v29, 1.0, v38
	v_rcp_f32_e32 v29, v29
	v_or_b32_e32 v30, 3, v30
	v_ashrrev_i32_e32 v31, 31, v30
	v_lshlrev_b64 v[30:31], 9, v[30:31]
	v_lshl_add_u64 v[30:31], v[32:33], 0, v[30:31]
	v_fma_f32 v29, v29, -2.0, 1.0
	global_store_dword v[30:31], v34, off sc1
	v_fma_f32 v30, -v29, v29, 1.0
	v_mul_f32_e32 v30, v129, v30
	v_cvt_pk_bf16_f32 v31, v30, s0
	v_mul_f32_e64 v30, v29, -v30
	v_cvt_pk_bf16_f32 v30, v30, s0
	ds_write_b16 v37, v30 offset:5168
	v_mov_b32_e32 v30, 0x1d800
	v_mul_f32_e32 v36, v129, v35
	v_lshl_or_b32 v32, v128, 6, v30
	v_mov_b32_e32 v30, v107
	ds_write_b16 v37, v31 offset:816
	v_mov_b32_e32 v31, 0
	v_mov_b32_dpp v30, v36 quad_perm:[1,0,3,2] row_mask:0xf bank_mask:0xf
	v_fmac_f32_e32 v30, v129, v35
	v_cmp_eq_u32_e32 vcc, 0, v1
	v_add_u32_e32 v26, v32, v26
	v_add_f32_dpp v30, v30, v30 quad_perm:[2,3,0,1] row_mask:0xf bank_mask:0xf bound_ctrl:1
	s_nop 1
	v_add_f32_dpp v30, v30, v30 row_half_mirror row_mask:0xf bank_mask:0xf bound_ctrl:1
	s_nop 1
	v_mov_b32_dpp v31, v30 row_mirror row_mask:0xf bank_mask:0xf
	s_and_saveexec_b64 s[4:5], vcc
	v_add_f32_e32 v30, v30, v31
	ds_write_b32 v26, v30
	s_or_b64 exec, exec, s[4:5]
	v_mul_f32_e32 v30, v129, v27
	v_mov_b32_e32 v31, 0
	s_nop 1
	v_mov_b32_dpp v31, v30 quad_perm:[1,0,3,2] row_mask:0xf bank_mask:0xf
	v_fmac_f32_e32 v31, v129, v27
	s_nop 1
	v_add_f32_dpp v27, v31, v31 quad_perm:[2,3,0,1] row_mask:0xf bank_mask:0xf bound_ctrl:1
	s_nop 1
	v_add_f32_dpp v27, v27, v27 row_half_mirror row_mask:0xf bank_mask:0xf bound_ctrl:1
	s_nop 1
	v_mov_b32_dpp v107, v27 row_mirror row_mask:0xf bank_mask:0xf
	s_and_saveexec_b64 s[4:5], vcc
	v_add_f32_e32 v27, v27, v107
	ds_write_b32 v26, v27 offset:4
	s_or_b64 exec, exec, s[4:5]
	v_mul_f32_e32 v30, v129, v28
	v_mov_b32_e32 v31, 0
	v_mov_b32_e32 v27, 0
	s_nop 0
	v_mov_b32_dpp v31, v30 quad_perm:[1,0,3,2] row_mask:0xf bank_mask:0xf
	v_fmac_f32_e32 v31, v129, v28
	v_mov_b32_e32 v30, 0
	s_nop 0
	v_add_f32_dpp v28, v31, v31 quad_perm:[2,3,0,1] row_mask:0xf bank_mask:0xf bound_ctrl:1
	s_nop 1
	v_add_f32_dpp v28, v28, v28 row_half_mirror row_mask:0xf bank_mask:0xf bound_ctrl:1
	s_nop 1
	v_mov_b32_dpp v30, v28 row_mirror row_mask:0xf bank_mask:0xf
	s_and_saveexec_b64 s[4:5], vcc
	v_add_f32_e32 v28, v28, v30
	ds_write_b32 v26, v28 offset:8
	s_or_b64 exec, exec, s[4:5]
	v_mul_f32_e32 v28, v129, v29
	v_mov_b32_e32 v30, 0
	s_nop 1
	v_mov_b32_dpp v30, v28 quad_perm:[1,0,3,2] row_mask:0xf bank_mask:0xf
	v_fmac_f32_e32 v30, v129, v29
	s_nop 1
	v_add_f32_dpp v28, v30, v30 quad_perm:[2,3,0,1] row_mask:0xf bank_mask:0xf bound_ctrl:1
	s_nop 1
	v_add_f32_dpp v28, v28, v28 row_half_mirror row_mask:0xf bank_mask:0xf bound_ctrl:1
	s_nop 1
	v_mov_b32_dpp v27, v28 row_mirror row_mask:0xf bank_mask:0xf
	s_and_saveexec_b64 s[4:5], vcc
	v_add_f32_e32 v27, v28, v27
	ds_write_b32 v26, v27 offset:12
	s_or_b64 exec, exec, s[4:5]
	s_mov_b64 s[4:5], 0
	s_branch .LBB0_28
.Lp_q:
	v_lshrrev_b32_e32 v234, 5, v0
	v_lshlrev_b32_e32 v234, 10, v234
	v_and_b32_e32 v239, 31, v0
	v_lshl_add_u32 v234, v239, 4, v234
	s_and_b32 s13, s2, 7
	s_lshl_b32 s14, s13, 14
	v_add_u32_e32 v239, s14, v234
	global_load_dwordx4 v[164:167], v239, s[28:29]
	s_add_i32 s13, s2, 1
	s_and_b32 s13, s13, 7
	s_lshl_b32 s14, s13, 14
	v_add_u32_e32 v239, s14, v234
	global_load_dwordx4 v[168:171], v239, s[28:29]
	s_add_i32 s13, s2, 2
	s_and_b32 s13, s13, 7
	s_lshl_b32 s14, s13, 14
	v_add_u32_e32 v239, s14, v234
	global_load_dwordx4 v[172:175], v239, s[28:29]
	s_add_i32 s13, s2, 3
	s_and_b32 s13, s13, 7
	s_lshl_b32 s14, s13, 14
	v_add_u32_e32 v239, s14, v234
	global_load_dwordx4 v[176:179], v239, s[28:29]
	s_add_i32 s13, s2, 4
	s_and_b32 s13, s13, 7
	s_lshl_b32 s14, s13, 14
	v_add_u32_e32 v239, s14, v234
	global_load_dwordx4 v[180:183], v239, s[28:29]
	s_add_i32 s13, s2, 5
	s_and_b32 s13, s13, 7
	s_lshl_b32 s14, s13, 14
	v_add_u32_e32 v239, s14, v234
	global_load_dwordx4 v[184:187], v239, s[28:29]
	s_add_i32 s13, s2, 6
	s_and_b32 s13, s13, 7
	s_lshl_b32 s14, s13, 14
	v_add_u32_e32 v239, s14, v234
	global_load_dwordx4 v[188:191], v239, s[28:29]
	s_add_i32 s13, s2, 7
	s_and_b32 s13, s13, 7
	s_lshl_b32 s14, s13, 14
	v_add_u32_e32 v239, s14, v234
	global_load_dwordx4 v[192:195], v239, s[28:29]
	s_waitcnt vmcnt(18)
	v_cvt_pk_bf16_f32 v12, v2, v3
	v_cvt_pk_bf16_f32 v13, v4, v5
	ds_write_b64 v238, v[12:13]
	s_waitcnt vmcnt(17)
	v_cvt_pk_bf16_f32 v6, v132, v133
	v_cvt_pk_bf16_f32 v7, v134, v135
	s_and_b32 s13, s2, 7
	s_mul_i32 s14, s13, 0x1100
	v_add_u32_e32 v239, s14, v58
	ds_write_b64 v239, v[6:7]
	s_waitcnt vmcnt(16)
	v_cvt_pk_bf16_f32 v8, v136, v137
	v_cvt_pk_bf16_f32 v9, v138, v139
	s_add_i32 s13, s2, 1
	s_and_b32 s13, s13, 7
	s_mul_i32 s14, s13, 0x1100
	v_add_u32_e32 v10, s14, v58
	ds_write_b64 v10, v[8:9]
	s_waitcnt vmcnt(15)
	v_cvt_pk_bf16_f32 v6, v140, v141
	v_cvt_pk_bf16_f32 v7, v142, v143
	s_add_i32 s13, s2, 2
	s_and_b32 s13, s13, 7
	s_mul_i32 s14, s13, 0x1100
	v_add_u32_e32 v239, s14, v58
	ds_write_b64 v239, v[6:7]
	s_waitcnt vmcnt(14)
	v_cvt_pk_bf16_f32 v8, v144, v145
	v_cvt_pk_bf16_f32 v9, v146, v147
	s_add_i32 s13, s2, 3
	s_and_b32 s13, s13, 7
	s_mul_i32 s14, s13, 0x1100
	v_add_u32_e32 v10, s14, v58
	ds_write_b64 v10, v[8:9]
	s_waitcnt vmcnt(13)
	v_cvt_pk_bf16_f32 v6, v148, v149
	v_cvt_pk_bf16_f32 v7, v150, v151
	s_add_i32 s13, s2, 4
	s_and_b32 s13, s13, 7
	s_mul_i32 s14, s13, 0x1100
	v_add_u32_e32 v239, s14, v58
	ds_write_b64 v239, v[6:7]
	s_waitcnt vmcnt(12)
	v_cvt_pk_bf16_f32 v8, v152, v153
	v_cvt_pk_bf16_f32 v9, v154, v155
	s_add_i32 s13, s2, 5
	s_and_b32 s13, s13, 7
	s_mul_i32 s14, s13, 0x1100
	v_add_u32_e32 v10, s14, v58
	ds_write_b64 v10, v[8:9]
	s_waitcnt vmcnt(11)
	v_cvt_pk_bf16_f32 v6, v156, v157
	v_cvt_pk_bf16_f32 v7, v158, v159
	s_add_i32 s13, s2, 6
	s_and_b32 s13, s13, 7
	s_mul_i32 s14, s13, 0x1100
	v_add_u32_e32 v239, s14, v58
	ds_write_b64 v239, v[6:7]
	s_waitcnt vmcnt(10)
	v_cvt_pk_bf16_f32 v8, v160, v161
	v_cvt_pk_bf16_f32 v9, v162, v163
	s_add_i32 s13, s2, 7
	s_and_b32 s13, s13, 7
	s_mul_i32 s14, s13, 0x1100
	v_add_u32_e32 v10, s14, v58
	ds_write_b64 v10, v[8:9]
	s_waitcnt vmcnt(7)
	v_cvt_pk_bf16_f32 v6, v164, v165
	v_cvt_pk_bf16_f32 v7, v166, v167
	s_and_b32 s13, s2, 7
	s_mul_i32 s14, s13, 0x1100
	s_add_i32 s14, s14, 34816
	v_add_u32_e32 v239, s14, v58
	ds_write_b64 v239, v[6:7]
	s_waitcnt vmcnt(6)
	v_cvt_pk_bf16_f32 v8, v168, v169
	v_cvt_pk_bf16_f32 v9, v170, v171
	s_add_i32 s13, s2, 1
	s_and_b32 s13, s13, 7
	s_mul_i32 s14, s13, 0x1100
	s_add_i32 s14, s14, 34816
	v_add_u32_e32 v10, s14, v58
	ds_write_b64 v10, v[8:9]
	s_waitcnt vmcnt(5)
	v_cvt_pk_bf16_f32 v6, v172, v173
	v_cvt_pk_bf16_f32 v7, v174, v175
	s_add_i32 s13, s2, 2
	s_and_b32 s13, s13, 7
	s_mul_i32 s14, s13, 0x1100
	s_add_i32 s14, s14, 34816
	v_add_u32_e32 v239, s14, v58
	ds_write_b64 v239, v[6:7]
	s_waitcnt vmcnt(4)
	v_cvt_pk_bf16_f32 v8, v176, v177
	v_cvt_pk_bf16_f32 v9, v178, v179
	s_add_i32 s13, s2, 3
	s_and_b32 s13, s13, 7
	s_mul_i32 s14, s13, 0x1100
	s_add_i32 s14, s14, 34816
	v_add_u32_e32 v10, s14, v58
	ds_write_b64 v10, v[8:9]
	s_waitcnt vmcnt(3)
	v_cvt_pk_bf16_f32 v6, v180, v181
	v_cvt_pk_bf16_f32 v7, v182, v183
	s_add_i32 s13, s2, 4
	s_and_b32 s13, s13, 7
	s_mul_i32 s14, s13, 0x1100
	s_add_i32 s14, s14, 34816
	v_add_u32_e32 v239, s14, v58
	ds_write_b64 v239, v[6:7]
	s_waitcnt vmcnt(2)
	v_cvt_pk_bf16_f32 v8, v184, v185
	v_cvt_pk_bf16_f32 v9, v186, v187
	s_add_i32 s13, s2, 5
	s_and_b32 s13, s13, 7
	s_mul_i32 s14, s13, 0x1100
	s_add_i32 s14, s14, 34816
	v_add_u32_e32 v10, s14, v58
	ds_write_b64 v10, v[8:9]
	s_waitcnt vmcnt(1)
	v_cvt_pk_bf16_f32 v6, v188, v189
	v_cvt_pk_bf16_f32 v7, v190, v191
	s_add_i32 s13, s2, 6
	s_and_b32 s13, s13, 7
	s_mul_i32 s14, s13, 0x1100
	s_add_i32 s14, s14, 34816
	v_add_u32_e32 v239, s14, v58
	ds_write_b64 v239, v[6:7]
	s_waitcnt vmcnt(0)
	v_cvt_pk_bf16_f32 v8, v192, v193
	v_cvt_pk_bf16_f32 v9, v194, v195
	s_add_i32 s13, s2, 7
	s_and_b32 s13, s13, 7
	s_mul_i32 s14, s13, 0x1100
	s_add_i32 s14, s14, 34816
	v_add_u32_e32 v10, s14, v58
	ds_write_b64 v10, v[8:9]
	s_waitcnt lgkmcnt(0)
	s_barrier
	global_load_dwordx4 v[2:5], v236, s[34:35] nt
	global_load_dwordx4 v[6:9], v236, s[34:35] offset:1024 nt
	global_load_dwordx4 v[10:13], v236, s[34:35] offset:2048 nt
	global_load_dwordx4 v[14:17], v236, s[34:35] offset:3072 nt
	ds_read_b128 v[28:31], v53
	ds_read_b128 v[60:63], v56
	ds_read_b128 v[32:35], v53 offset:64
	ds_read_b128 v[64:67], v56 offset:64
	ds_read_b128 v[36:39], v53 offset:128
	ds_read_b128 v[68:71], v56 offset:128
	ds_read_b128 v[40:43], v53 offset:192
	ds_read_b128 v[72:75], v56 offset:192
	s_waitcnt lgkmcnt(6)
	v_mfma_f32_16x16x32_bf16 v[18:21], v[28:31], v[60:63], 0
	s_waitcnt lgkmcnt(4)
	v_mfma_f32_16x16x32_bf16 v[18:21], v[32:35], v[64:67], v[18:21]
	s_waitcnt lgkmcnt(2)
	v_mfma_f32_16x16x32_bf16 v[18:21], v[36:39], v[68:71], v[18:21]
	s_waitcnt lgkmcnt(0)
	v_mfma_f32_16x16x32_bf16 v[18:21], v[40:43], v[72:75], v[18:21]
	s_nop 7
	v_mul_f32_e32 v18, s44, v18
	v_mul_f32_e32 v19, s44, v19
	v_mul_f32_e32 v20, s44, v20
	v_mul_f32_e32 v21, s44, v21
	v_cvt_pk_bf16_f32 v18, v18, v18
	v_cvt_pk_bf16_f32 v19, v19, v19
	v_cvt_pk_bf16_f32 v20, v20, v20
	v_cvt_pk_bf16_f32 v21, v21, v21
	ds_write_b16 v55, v18
	ds_write_b16 v55, v19 offset:272
	ds_write_b16 v55, v20 offset:544
	ds_write_b16 v55, v21 offset:816
	s_waitcnt lgkmcnt(0)
	s_barrier
	ds_read_b128 v[28:31], v54
	ds_read_b128 v[60:63], v57
	ds_read_b128 v[32:35], v54 offset:64
	ds_read_b128 v[64:67], v57 offset:64
	ds_read_b128 v[36:39], v54 offset:128
	ds_read_b128 v[68:71], v57 offset:128
	ds_read_b128 v[40:43], v54 offset:192
	ds_read_b128 v[72:75], v57 offset:192
	s_waitcnt lgkmcnt(6)
	v_mfma_f32_16x16x32_bf16 v[18:21], v[28:31], v[60:63], 0
	s_waitcnt lgkmcnt(4)
	v_mfma_f32_16x16x32_bf16 v[18:21], v[32:35], v[64:67], v[18:21]
	s_waitcnt lgkmcnt(2)
	v_mfma_f32_16x16x32_bf16 v[18:21], v[36:39], v[68:71], v[18:21]
	s_waitcnt lgkmcnt(0)
	v_mfma_f32_16x16x32_bf16 v[18:21], v[40:43], v[72:75], v[18:21]
	s_load_dwordx2 s[4:5], s[0:1], 0x68
	v_lshl_or_b32 v26, v24, 2, s12
	v_mov_b32_e32 v107, 0
	v_ashrrev_i32_e32 v27, 31, v26
	v_lshlrev_b64 v[28:29], 9, v[26:27]
	s_waitcnt lgkmcnt(0)
	v_lshl_add_u64 v[30:31], s[4:5], 0, v[106:107]
	v_lshl_add_u64 v[28:29], v[30:31], 0, v[28:29]
	v_mul_u32_u24_e32 v24, 0x440, v24
	s_mov_b32 s4, 0x19200
	global_store_dword v[28:29], v18, off sc1
	v_add3_u32 v28, v24, v25, s4
	v_mul_f32_e32 v24, v18, v18
	v_cvt_pk_bf16_f32 v27, v18, s0
	v_cvt_pk_bf16_f32 v24, v24, s0
	ds_write_b16 v28, v27
	ds_write_b16 v28, v24 offset:4352
	v_max3_f32 v27, |v18|, 0, |v19|
	v_or_b32_e32 v24, 1, v26
	v_cvt_pk_bf16_f32 v18, v19, s0
	v_ashrrev_i32_e32 v25, 31, v24
	ds_write_b16 v28, v18 offset:272
	v_mul_f32_e32 v18, v19, v19
	v_lshlrev_b64 v[24:25], 9, v[24:25]
	v_cvt_pk_bf16_f32 v18, v18, s0
	v_lshl_add_u64 v[24:25], v[30:31], 0, v[24:25]
	ds_write_b16 v28, v18 offset:4624
	v_or_b32_e32 v18, 2, v26
	global_store_dword v[24:25], v19, off sc1
	v_ashrrev_i32_e32 v19, 31, v18
	v_lshlrev_b64 v[18:19], 9, v[18:19]
	v_lshl_add_u64 v[18:19], v[30:31], 0, v[18:19]
	global_store_dword v[18:19], v20, off sc1
	v_cvt_pk_bf16_f32 v18, v20, s0
	ds_write_b16 v28, v18 offset:544
	v_mul_f32_e32 v18, v20, v20
	v_cvt_pk_bf16_f32 v18, v18, s0
	ds_write_b16 v28, v18 offset:4896
	v_or_b32_e32 v18, 3, v26
	v_ashrrev_i32_e32 v19, 31, v18
	v_lshlrev_b64 v[18:19], 9, v[18:19]
	v_lshl_add_u64 v[18:19], v[30:31], 0, v[18:19]
	global_store_dword v[18:19], v21, off sc1
	v_cvt_pk_bf16_f32 v18, v21, s0
	ds_write_b16 v28, v18 offset:816
	v_mul_f32_e32 v18, v21, v21
	v_cvt_pk_bf16_f32 v18, v18, s0
	v_max3_f32 v20, v27, |v20|, |v21|
	ds_write_b16 v28, v18 offset:5168
	v_mov_b32_e32 v18, v107
	v_mov_b32_e32 v19, v107
	v_cmp_eq_u32_e32 vcc, 0, v126
	v_mov_b32_dpp v18, v20 quad_perm:[1,0,3,2] row_mask:0xf bank_mask:0xf
	v_max_f32_e32 v18, v18, v18
	v_max_f32_e32 v18, v20, v18
	s_nop 1
	v_mov_b32_dpp v19, v18 quad_perm:[2,3,0,1] row_mask:0xf bank_mask:0xf
	v_max_f32_e32 v19, v19, v19
	v_max_f32_e32 v18, v18, v19
	v_mov_b32_e32 v19, v107
	s_nop 1
	v_mov_b32_dpp v19, v18 row_half_mirror row_mask:0xf bank_mask:0xf
	v_max_f32_e32 v19, v19, v19
	v_max_f32_e32 v18, v18, v19
	v_mov_b32_e32 v19, v107
	s_nop 1
	v_mov_b32_dpp v19, v18 row_mirror row_mask:0xf bank_mask:0xf
	v_max_f32_e32 v19, v19, v19
	v_max_f32_e32 v18, v18, v19
	s_nop 0
	v_readlane_b32 s8, v18, 0
	v_readlane_b32 s9, v18, 16
	v_readlane_b32 s10, v18, 32
	v_readlane_b32 s11, v18, 48
	v_and_b32_e32 v18, 0x7fffffff, v129
	s_nop 1
	v_add_f32_dpp v18, v18, |v129| quad_perm:[1,0,3,2] row_mask:0xf bank_mask:0xf bound_ctrl:1
	s_nop 1
	v_add_f32_dpp v18, v18, v18 quad_perm:[2,3,0,1] row_mask:0xf bank_mask:0xf bound_ctrl:1
	s_nop 1
	v_add_f32_dpp v18, v18, v18 row_half_mirror row_mask:0xf bank_mask:0xf bound_ctrl:1
	s_nop 1
	v_mov_b32_dpp v107, v18 row_mirror row_mask:0xf bank_mask:0xf
	s_and_saveexec_b64 s[4:5], vcc
	s_cbranch_execz .LBB0_27
	v_mov_b32_e32 v19, 0x1d800
	v_lshl_or_b32 v20, v128, 6, v19
	v_add_f32_e32 v19, v18, v107
	v_max_f32_e64 v18, s11, s11
	v_max_f32_e64 v21, s10, s10
	v_max_f32_e32 v18, v21, v18
	v_mov_b32_e32 v21, s9
	v_max3_f32 v18, s8, v21, v18
	ds_write_b64 v20, v[18:19]
